# S3 RET state loads issued together; HG onorm loads hoisted (S3+S1 heavy)
# speedup vs baseline: 1.0082x; 1.0082x over previous
.LBB0_455:
	v_add_u32_e32 v8, s3, v8
	v_cvt_pk_bf16_f32 v20, v13, v10
	v_lshlrev_b32_e32 v10, 4, v8
	v_and_b32_e32 v10, 0xfffffc00, v10
	v_bitop3_b32 v8, v8, v9, 56 bitop3:0x6c
	v_add3_u32 v8, v11, v10, v8
	v_cvt_pk_bf16_f32 v21, v14, v15
	ds_write_b64 v8, v[20:21]
	s_waitcnt lgkmcnt(0)
	s_barrier
	v_add_u32_e32 v8, s23, v12
	v_add_u32_e32 v12, s24, v12
	v_add_u32_e32 v119, s67, v18
	ds_read_b128 v[8:11], v8
	ds_read_b128 v[12:15], v12
	ds_read_b128 v[20:23], v17
	ds_read_b128 v[24:27], v119
	ds_read_b128 v[28:31], v119 offset:4096
	ds_read_b128 v[32:35], v119 offset:8192
	ds_read_b128 v[36:39], v119 offset:12288
	ds_read_b128 v[40:43], v17 offset:1024
	ds_read_b128 v[44:47], v119 offset:1024
	ds_read_b128 v[48:51], v119 offset:5120
	ds_read_b128 v[52:55], v119 offset:9216
	ds_read_b128 v[56:59], v119 offset:13312
	v_add_u32_e32 v120, s29, v18
	v_add_u32_e32 v121, s69, v18
	v_add_u32_e32 v140, s68, v18
	ds_read_b128 v[60:63], v17 offset:2048
	ds_read_b128 v[144:147], v119 offset:2048
	ds_read_b128 v[148:151], v119 offset:6144
	ds_read_b128 v[152:155], v119 offset:10240
	ds_read_b128 v[188:191], v119 offset:14336
	s_waitcnt lgkmcnt(13)
	v_mfma_f32_16x16x32_bf16 v[24:27], v[24:27], v[20:23], 0
	s_waitcnt lgkmcnt(12)
	v_mfma_f32_16x16x32_bf16 v[28:31], v[28:31], v[20:23], 0
	s_waitcnt lgkmcnt(11)
	v_mfma_f32_16x16x32_bf16 v[32:35], v[32:35], v[20:23], 0
	s_waitcnt lgkmcnt(10)
	v_mfma_f32_16x16x32_bf16 v[18:21], v[36:39], v[20:23], 0
	s_waitcnt lgkmcnt(8)
	v_mfma_f32_16x16x32_bf16 v[22:25], v[44:47], v[40:43], v[24:27]
	ds_read_b128 v[36:39], v17 offset:3072
	s_waitcnt lgkmcnt(8)
	v_mfma_f32_16x16x32_bf16 v[26:29], v[48:51], v[40:43], v[28:31]
	s_waitcnt lgkmcnt(7)
	v_mfma_f32_16x16x32_bf16 v[30:33], v[52:55], v[40:43], v[32:35]
	ds_read_b128 v[44:47], v119 offset:3072
	ds_read_b128 v[48:51], v119 offset:7168
	ds_read_b128 v[52:55], v119 offset:11264
	ds_read_b128 v[192:195], v119 offset:15360
	s_waitcnt lgkmcnt(10)
	v_mfma_f32_16x16x32_bf16 v[18:21], v[56:59], v[40:43], v[18:21]
	s_waitcnt lgkmcnt(8)
	v_mfma_f32_16x16x32_bf16 v[22:25], v[144:147], v[60:63], v[22:25]
	ds_read_b128 v[40:43], v120
	ds_read_b128 v[56:59], v140 offset:49152
	s_waitcnt lgkmcnt(9)
	v_mfma_f32_16x16x32_bf16 v[26:29], v[148:151], v[60:63], v[26:29]
	s_waitcnt lgkmcnt(8)
	v_mfma_f32_16x16x32_bf16 v[30:33], v[152:155], v[60:63], v[30:33]
	ds_read_b128 v[144:147], v140 offset:51200
	ds_read_b128 v[148:151], v140 offset:53248
	ds_read_b128 v[152:155], v140 offset:55296
	s_waitcnt lgkmcnt(10)
	v_mfma_f32_16x16x32_bf16 v[18:21], v[188:191], v[60:63], v[18:21]
	s_waitcnt lgkmcnt(8)
	v_mfma_f32_16x16x32_bf16 v[22:25], v[44:47], v[36:39], v[22:25]
	s_waitcnt lgkmcnt(7)
	v_mfma_f32_16x16x32_bf16 v[26:29], v[48:51], v[36:39], v[26:29]
	ds_read_b128 v[44:47], v120 offset:1024
	ds_read_b128 v[48:51], v140 offset:50176
	s_waitcnt lgkmcnt(8)
	v_mfma_f32_16x16x32_bf16 v[30:33], v[52:55], v[36:39], v[30:33]
	ds_read_b128 v[52:55], v140 offset:52224
	ds_read_b128 v[188:191], v140 offset:54272
	ds_read_b128 v[212:215], v140 offset:56320
	s_waitcnt lgkmcnt(10)
	v_mfma_f32_16x16x32_bf16 v[18:21], v[192:195], v[36:39], v[18:21]
	s_waitcnt lgkmcnt(7)
	v_mfma_f32_16x16x32_bf16 v[26:29], v[144:147], v[40:43], v[26:29]
	ds_read_b128 v[144:147], v121 offset:32768
	ds_read_b128 v[192:195], v121 offset:33792
	s_waitcnt lgkmcnt(8)
	v_mfma_f32_16x16x32_bf16 v[30:33], v[148:151], v[40:43], v[30:33]
	ds_read_b128 v[34:37], v16 offset:49152
	ds_read_b128 v[148:151], v16 offset:50176
	ds_read_b128 v[216:219], v16 offset:51200
	ds_read_b128 v[220:223], v16 offset:52224
	v_mfma_f32_16x16x32_bf16 v[22:25], v[56:59], v[40:43], v[22:25]
	s_waitcnt lgkmcnt(11)
	v_mfma_f32_16x16x32_bf16 v[18:21], v[152:155], v[40:43], v[18:21]
	s_waitcnt lgkmcnt(9)
	v_mfma_f32_16x16x32_bf16 v[60:63], v[48:51], v[44:47], v[22:25]
	s_waitcnt lgkmcnt(8)
	v_mfma_f32_16x16x32_bf16 v[56:59], v[52:55], v[44:47], v[26:29]
	s_waitcnt lgkmcnt(7)
	v_mfma_f32_16x16x32_bf16 v[48:51], v[188:191], v[44:47], v[30:33]
	ds_read_b128 v[22:25], v16 offset:53248
	ds_read_b128 v[26:29], v16 offset:54272
	ds_read_b128 v[152:155], v16 offset:55296
	ds_read_b128 v[188:191], v16 offset:56320
	s_waitcnt lgkmcnt(10)
	v_mfma_f32_16x16x32_bf16 v[52:55], v[212:215], v[44:47], v[18:21]
	s_waitcnt lgkmcnt(7)
	v_mfma_f32_16x16x32_bf16 v[18:21], v[144:147], v[34:37], 0
	s_waitcnt lgkmcnt(6)
	v_mfma_f32_16x16x32_bf16 v[44:47], v[192:195], v[148:151], v[18:21]
	s_waitcnt lgkmcnt(5)
	v_mfma_f32_16x16x32_bf16 v[18:21], v[144:147], v[216:219], 0
	s_waitcnt lgkmcnt(4)
	v_mfma_f32_16x16x32_bf16 v[40:43], v[192:195], v[220:223], v[18:21]
	s_waitcnt lgkmcnt(3)
	v_mfma_f32_16x16x32_bf16 v[18:21], v[144:147], v[22:25], 0
	s_waitcnt lgkmcnt(2)
	v_mfma_f32_16x16x32_bf16 v[32:35], v[192:195], v[26:29], v[18:21]
	s_nop 5
	ds_read_b128 v[18:21], v16 offset:57344
	ds_read_b128 v[22:25], v16 offset:58368
	ds_read_b128 v[148:151], v16 offset:59392
	ds_read_b128 v[212:215], v16 offset:60416
	s_waitcnt lgkmcnt(5)
	v_mfma_f32_16x16x32_bf16 v[26:29], v[144:147], v[152:155], 0
	ds_read_b128 v[152:155], v16 offset:61440
	ds_read_b128 v[216:219], v16 offset:62464
	ds_read_b128 v[220:223], v16 offset:63488
	ds_read_b128 v[224:227], v16 offset:64512
	s_waitcnt lgkmcnt(8)
	v_mfma_f32_16x16x32_bf16 v[36:39], v[192:195], v[188:191], v[26:29]
	s_waitcnt lgkmcnt(7)
	v_mfma_f32_16x16x32_bf16 v[16:19], v[144:147], v[18:21], 0
	s_mov_b64 s[60:61], -1
	s_andn2_b64 vcc, exec, s[58:59]
	s_waitcnt lgkmcnt(6)
	v_mfma_f32_16x16x32_bf16 v[28:31], v[192:195], v[22:25], v[16:19]
	s_waitcnt lgkmcnt(5)
	v_mfma_f32_16x16x32_bf16 v[16:19], v[144:147], v[148:151], 0
	s_waitcnt lgkmcnt(4)
	v_mfma_f32_16x16x32_bf16 v[24:27], v[192:195], v[212:215], v[16:19]
	s_waitcnt lgkmcnt(3)
	v_mfma_f32_16x16x32_bf16 v[16:19], v[144:147], v[152:155], 0
	s_waitcnt lgkmcnt(2)
	v_mfma_f32_16x16x32_bf16 v[20:23], v[192:195], v[216:219], v[16:19]
	s_waitcnt lgkmcnt(1)
	v_mfma_f32_16x16x32_bf16 v[16:19], v[144:147], v[220:223], 0
	s_waitcnt lgkmcnt(0)
	v_mfma_f32_16x16x32_bf16 v[16:19], v[192:195], v[224:227], v[16:19]
	s_cbranch_vccnz .LBB0_459
	s_waitcnt vmcnt(1)
	v_lshlrev_b32_e32 v120, 16, v0
	v_and_b32_e32 v121, 0xffff0000, v0
	v_lshlrev_b32_e32 v140, 16, v1
	v_and_b32_e32 v141, 0xffff0000, v1
	v_pk_add_f32 v[154:155], v[62:63], v[140:141]
	v_pk_add_f32 v[156:157], v[60:61], v[120:121]
	v_mul_f32_e32 v120, v155, v155
	v_mul_f32_e32 v119, v157, v157
	v_fmac_f32_e32 v119, v156, v156
	v_fmac_f32_e32 v120, v154, v154
	v_add_f32_e32 v119, v119, v120
	v_lshlrev_b32_e32 v120, 16, v2
	v_and_b32_e32 v121, 0xffff0000, v2
	v_lshlrev_b32_e32 v140, 16, v3
	v_and_b32_e32 v141, 0xffff0000, v3
	v_pk_add_f32 v[148:149], v[58:59], v[140:141]
	v_pk_add_f32 v[150:151], v[56:57], v[120:121]
	v_mul_f32_e32 v121, v149, v149
	v_mul_f32_e32 v120, v151, v151
	v_fmac_f32_e32 v120, v150, v150
	v_fmac_f32_e32 v121, v148, v148
	v_add_f32_e32 v120, v120, v121
	v_add_f32_e32 v119, v119, v120
	s_waitcnt vmcnt(0)
	v_lshlrev_b32_e32 v120, 16, v4
	v_and_b32_e32 v121, 0xffff0000, v4
	v_lshlrev_b32_e32 v140, 16, v5
	v_and_b32_e32 v141, 0xffff0000, v5
	v_pk_add_f32 v[144:145], v[50:51], v[140:141]
	v_pk_add_f32 v[146:147], v[48:49], v[120:121]
	v_mul_f32_e32 v121, v145, v145
	v_mul_f32_e32 v120, v147, v147
	v_fmac_f32_e32 v120, v146, v146
	v_fmac_f32_e32 v121, v144, v144
	v_add_f32_e32 v120, v120, v121
	v_add_f32_e32 v119, v119, v120
	v_lshlrev_b32_e32 v140, 16, v6
	v_and_b32_e32 v141, 0xffff0000, v6
	v_lshlrev_b32_e32 v120, 16, v7
	v_and_b32_e32 v121, 0xffff0000, v7
	v_pk_add_f32 v[120:121], v[54:55], v[120:121]
	v_pk_add_f32 v[140:141], v[52:53], v[140:141]
	v_mul_f32_e32 v152, v121, v121
	v_mul_f32_e32 v142, v141, v141
	v_fmac_f32_e32 v142, v140, v140
	v_fmac_f32_e32 v152, v120, v120
	v_add_f32_e32 v142, v142, v152
	v_add_f32_e32 v119, v119, v142
	v_lshlrev_b32_e32 v142, 2, v186
	v_xor_b32_e32 v152, 64, v142
	ds_bpermute_b32 v152, v152, v119
	v_xor_b32_e32 v142, 0x80, v142
	v_cmp_gt_u32_e32 vcc, 16, v186
	s_and_b32 s39, s63, 0x80
	s_waitcnt lgkmcnt(0)
	v_add_f32_e32 v119, v119, v152
	ds_bpermute_b32 v142, v142, v119
	s_waitcnt lgkmcnt(0)
	v_add_f32_e32 v119, v119, v142
	s_and_saveexec_b64 s[60:61], vcc
	s_add_i32 vcc_lo, s39, s71
	v_or_b32_e32 v142, vcc_lo, v117
	v_lshl_add_u32 v142, v142, 2, s70
	ds_write_b32 v142, v119
	s_or_b64 exec, exec, s[60:61]
	s_add_i32 s39, s39, s80
	v_or_b32_e32 v117, s39, v117
	s_waitcnt lgkmcnt(0)
	s_barrier
	v_lshl_add_u32 v117, v117, 2, s70
	ds_read_b32 v117, v117
	s_mov_b64 s[60:61], 0
	s_waitcnt lgkmcnt(0)
	v_add_f32_e32 v117, v119, v117
	v_fmamk_f32 v117, v117, 0x3c000000, v200
	v_rsq_f32_e32 v142, v117
	v_ashrrev_i32_e32 v117, 31, v116
	v_lshlrev_b64 v[152:153], 2, v[116:117]
	v_lshl_add_u64 v[192:193], s[52:53], 0, v[152:153]
	global_load_dwordx4 v[188:191], v[192:193], off
	global_load_dwordx4 v[212:215], v[192:193], off offset:64
	global_load_dwordx4 v[216:219], v[192:193], off offset:128
	v_lshl_add_u64 v[224:225], s[54:55], 0, v[152:153]
	global_load_dwordx4 v[220:223], v[224:225], off
	v_ashrrev_i32_e32 v119, 31, v118
	v_pk_mul_f32 v[154:155], v[154:155], v[142:143] op_sel_hi:[1,0]
	v_pk_mul_f32 v[156:157], v[156:157], v[142:143] op_sel_hi:[1,0]
	v_lshlrev_b64 v[118:119], 11, v[118:119]
	v_lshl_add_u64 v[118:119], s[50:51], 0, v[118:119]
	v_lshlrev_b64 v[116:117], 1, v[116:117]
	v_pk_mul_f32 v[150:151], v[150:151], v[142:143] op_sel_hi:[1,0]
	v_pk_mul_f32 v[148:149], v[148:149], v[142:143] op_sel_hi:[1,0]
	v_pk_mul_f32 v[144:145], v[144:145], v[142:143] op_sel_hi:[1,0]
	v_pk_mul_f32 v[146:147], v[146:147], v[142:143] op_sel_hi:[1,0]
	v_pk_mul_f32 v[140:141], v[140:141], v[142:143] op_sel_hi:[1,0]
	v_pk_mul_f32 v[120:121], v[120:121], v[142:143] op_sel_hi:[1,0]
	s_waitcnt vmcnt(3)
	v_pk_mul_f32 v[154:155], v[190:191], v[154:155]
	v_pk_mul_f32 v[156:157], v[188:189], v[156:157]
	v_lshlrev_b32_e32 v188, 16, v78
	v_and_b32_e32 v189, 0xffff0000, v78
	v_lshlrev_b32_e32 v190, 16, v79
	v_and_b32_e32 v191, 0xffff0000, v79
	v_pk_mul_f32 v[154:155], v[154:155], v[190:191]
	v_pk_mul_f32 v[156:157], v[156:157], v[188:189]
	s_nop 0
	v_cvt_pk_bf16_f32 v156, v156, v157
	v_cvt_pk_bf16_f32 v157, v154, v155
	v_lshl_add_u64 v[154:155], s[42:43], 1, v[118:119]
	v_lshl_add_u64 v[188:189], v[154:155], 0, v[116:117]
	global_store_dwordx2 v[188:189], v[156:157], off
	v_lshl_add_u64 v[118:119], s[44:45], 1, v[118:119]
	v_lshl_add_u64 v[116:117], v[118:119], 0, v[116:117]
	s_waitcnt vmcnt(3)
	v_pk_mul_f32 v[150:151], v[212:213], v[150:151]
	v_lshlrev_b32_e32 v154, 16, v76
	v_and_b32_e32 v155, 0xffff0000, v76
	v_pk_mul_f32 v[148:149], v[214:215], v[148:149]
	v_lshlrev_b32_e32 v156, 16, v77
	v_and_b32_e32 v157, 0xffff0000, v77
	v_pk_mul_f32 v[150:151], v[150:151], v[154:155]
	v_pk_mul_f32 v[148:149], v[148:149], v[156:157]
	v_cvt_pk_bf16_f32 v150, v150, v151
	s_nop 0
	v_cvt_pk_bf16_f32 v151, v148, v149
	global_store_dwordx2 v[188:189], v[150:151], off offset:32
	s_waitcnt vmcnt(3)
	v_pk_mul_f32 v[144:145], v[144:145], v[218:219]
	v_pk_mul_f32 v[146:147], v[146:147], v[216:217]
	v_lshlrev_b32_e32 v148, 16, v74
	v_and_b32_e32 v149, 0xffff0000, v74
	v_lshlrev_b32_e32 v150, 16, v75
	v_and_b32_e32 v151, 0xffff0000, v75
	v_pk_mul_f32 v[144:145], v[144:145], v[150:151]
	v_pk_mul_f32 v[146:147], v[146:147], v[148:149]
	s_nop 0
	v_cvt_pk_bf16_f32 v146, v146, v147
	v_cvt_pk_bf16_f32 v147, v144, v145
	global_store_dwordx2 v[188:189], v[146:147], off offset:64
	s_waitcnt vmcnt(3)
	v_pk_mul_f32 v[140:141], v[140:141], v[220:221]
	v_lshlrev_b32_e32 v144, 16, v72
	v_and_b32_e32 v145, 0xffff0000, v72
	v_pk_mul_f32 v[120:121], v[120:121], v[222:223]
	v_lshlrev_b32_e32 v146, 16, v73
	v_and_b32_e32 v147, 0xffff0000, v73
	v_pk_mul_f32 v[140:141], v[140:141], v[144:145]
	v_pk_mul_f32 v[120:121], v[120:121], v[146:147]
	v_cvt_pk_bf16_f32 v140, v140, v141
	s_nop 0
	v_cvt_pk_bf16_f32 v141, v120, v121
	global_store_dwordx2 v[116:117], v[140:141], off

.LBB0_702:
	s_lshl_b32 s20, s75, 2
	s_or_b32 s78, s20, s59
	s_lshl_b64 s[20:21], s[78:79], 2
	v_readlane_b32 s42, v241, 59
	s_add_u32 s20, s42, s20
	v_readlane_b32 s42, v241, 61
	s_addc_u32 s21, s42, s21
	global_load_dword v8, v65, s[20:21]
	s_mov_b32 s20, 0xc2ce8ed0
	s_mov_b32 s43, s75
	v_readlane_b32 s52, v241, 55
	s_mov_b32 s53, s79
	s_mov_b32 s84, 0
	v_readlane_b32 s72, v241, 51
	s_mov_b32 s83, 1
	s_waitcnt vmcnt(0)
	v_mul_f32_e32 v9, 0x3fb8aa3b, v8
	v_fma_f32 v10, v8, s94, -v9
	v_rndne_f32_e32 v11, v9
	v_fmac_f32_e32 v10, 0x32a5705f, v8
	v_sub_f32_e32 v9, v9, v11
	v_add_f32_e32 v9, v9, v10
	v_exp_f32_e32 v9, v9
	v_cvt_i32_f32_e32 v10, v11
	v_cmp_ngt_f32_e32 vcc, s20, v8
	s_mov_b32 s20, 0x42b17218
	v_ldexp_f32 v9, v9, v10
	v_cndmask_b32_e32 v9, 0, v9, vcc
	v_cmp_nlt_f32_e32 vcc, s20, v8
	s_add_i32 s20, s75, s76
	s_mul_hi_i32 s21, s20, 0x41
	v_cndmask_b32_e32 v64, v204, v9, vcc
	v_mul_f32_e32 v8, 0xc2800000, v64
	v_mul_f32_e32 v8, 0x3fb8aa3b, v8
	v_exp_f32_e32 v84, v8
	v_add_co_u32_e64 v8, s[48:49], s43, -1
	s_nop 0
	v_readfirstlane_b32 s75, v8
	v_cndmask_b32_e64 v8, 0, 1, s[48:49]
	v_readlane_b32 s48, v242, 58
	v_mov_b32_e32 v9, s79
	v_readlane_b32 s49, v242, 59
	s_mulk_i32 s20, 0x41
	s_cmp_lg_u32 s43, 0
	v_lshl_add_u64 v[8:9], v[8:9], 0, s[48:49]
	v_lshl_add_u64 v[8:9], v[8:9], 0, s[20:21]
	v_readlane_b32 s20, v242, 60
	v_lshlrev_b64 v[8:9], 15, v[8:9]
	v_readlane_b32 s21, v242, 61
	s_cselect_b64 s[48:49], -1, 0
	s_cmp_eq_u32 s43, 0
	v_lshl_add_u64 v[8:9], s[20:21], 0, v[8:9]
	v_lshl_add_u64 v[10:11], v[8:9], 0, v[68:69]
	global_load_dwordx2 v[88:89], v[10:11], off nt
	v_lshl_add_u64 v[10:11], v[8:9], 0, v[70:71]
	global_load_dwordx2 v[92:93], v[10:11], off nt
	v_lshl_add_u64 v[10:11], v[8:9], 0, v[72:73]
	global_load_dwordx2 v[96:97], v[10:11], off nt
	v_lshl_add_u64 v[10:11], v[8:9], 0, v[74:75]
	global_load_dwordx2 v[100:101], v[10:11], off nt
	v_lshl_add_u64 v[10:11], v[8:9], 0, v[76:77]
	global_load_dwordx2 v[104:105], v[10:11], off nt
	v_lshl_add_u64 v[10:11], v[8:9], 0, v[78:79]
	global_load_dwordx2 v[108:109], v[10:11], off nt
	v_lshl_add_u64 v[10:11], v[8:9], 0, v[80:81]
	global_load_dwordx2 v[112:113], v[10:11], off nt
	v_lshl_add_u64 v[10:11], v[8:9], 0, v[82:83]
	global_load_dwordx2 v[116:117], v[10:11], off nt
	s_cselect_b64 s[20:21], -1, 0
	s_and_b64 s[50:51], s[20:21], exec
	v_readlane_b32 s50, v241, 45
	v_readlane_b32 s51, v241, 19
	s_cselect_b32 s77, s50, s51
	v_readlane_b32 s50, v241, 23
	v_readlane_b32 s51, v241, 21
	s_cselect_b32 s88, s50, s51
	v_readlane_b32 s50, v241, 27
	v_readlane_b32 s51, v241, 25
	s_cselect_b32 s85, s50, s51
	v_readlane_b32 s50, v241, 31
	v_readlane_b32 s51, v241, 29
	s_cselect_b32 s92, s50, s51
	v_readlane_b32 s50, v241, 35
	v_readlane_b32 s51, v241, 33
	s_cselect_b32 s89, s50, s51
	v_readlane_b32 s50, v241, 39
	v_readlane_b32 s51, v241, 37
	s_cselect_b32 s96, s50, s51
	v_readlane_b32 s50, v241, 43
	v_readlane_b32 s51, v241, 41
	s_cselect_b32 s42, 0, 0x1c0
	s_cselect_b32 s93, s50, s51
	v_readlane_b32 s50, v241, 49
	v_readlane_b32 s51, v241, 47
	s_cselect_b32 s58, s50, s51
	s_add_i32 s42, s42, s74
	s_add_i32 s50, s42, s77
	s_lshl_b32 s78, s73, 1
	s_lshl_b32 s52, s52, 1
	s_add_i32 s54, s42, s88
	v_mov_b32_e32 v118, v84
	v_mov_b32_e32 v119, v84
	v_mad_i64_i32 v[8:9], s[50:51], s50, v205, v[66:67]
	v_lshl_add_u64 v[10:11], v[8:9], 0, s[78:79]
	s_lshl_b32 s50, s71, 1
	s_mov_b32 s51, s79
	global_load_dword v140, v[10:11], off
	v_lshl_add_u64 v[10:11], v[8:9], 0, s[50:51]
	v_lshl_add_u64 v[8:9], v[8:9], 0, s[52:53]
	global_load_dword v141, v[10:11], off
	global_load_dword v142, v[8:9], off
	v_mad_i64_i32 v[8:9], s[54:55], s54, v205, v[66:67]
	v_lshl_add_u64 v[10:11], v[8:9], 0, s[78:79]
	global_load_dword v143, v[10:11], off
	v_lshl_add_u64 v[10:11], v[8:9], 0, s[50:51]
	v_lshl_add_u64 v[8:9], v[8:9], 0, s[52:53]
	s_add_i32 s54, s42, s85
	global_load_dword v144, v[10:11], off
	global_load_dword v145, v[8:9], off
	v_mad_i64_i32 v[8:9], s[54:55], s54, v205, v[66:67]
	v_lshl_add_u64 v[10:11], v[8:9], 0, s[78:79]
	global_load_dword v166, v[10:11], off
	v_lshl_add_u64 v[10:11], v[8:9], 0, s[50:51]
	v_lshl_add_u64 v[8:9], v[8:9], 0, s[52:53]
	s_add_i32 s54, s42, s92
	global_load_dword v167, v[10:11], off
	global_load_dword v168, v[8:9], off
	v_mad_i64_i32 v[8:9], s[54:55], s54, v205, v[66:67]
	v_lshl_add_u64 v[10:11], v[8:9], 0, s[78:79]
	global_load_dword v169, v[10:11], off
	v_lshl_add_u64 v[10:11], v[8:9], 0, s[50:51]
	v_lshl_add_u64 v[8:9], v[8:9], 0, s[52:53]
	s_add_i32 s54, s42, s89
	global_load_dword v170, v[10:11], off
	global_load_dword v171, v[8:9], off
	v_mad_i64_i32 v[8:9], s[54:55], s54, v205, v[66:67]
	v_lshl_add_u64 v[10:11], v[8:9], 0, s[78:79]
	global_load_dword v172, v[10:11], off
	v_lshl_add_u64 v[10:11], v[8:9], 0, s[50:51]
	v_lshl_add_u64 v[8:9], v[8:9], 0, s[52:53]
	s_add_i32 s54, s42, s96
	global_load_dword v173, v[10:11], off
	global_load_dword v174, v[8:9], off
	v_mad_i64_i32 v[8:9], s[54:55], s54, v205, v[66:67]
	v_lshl_add_u64 v[10:11], v[8:9], 0, s[78:79]
	global_load_dword v175, v[10:11], off
	v_lshl_add_u64 v[10:11], v[8:9], 0, s[50:51]
	v_lshl_add_u64 v[8:9], v[8:9], 0, s[52:53]
	s_add_i32 s54, s42, s93
	global_load_dword v176, v[10:11], off
	global_load_dword v177, v[8:9], off
	v_mad_i64_i32 v[8:9], s[54:55], s54, v205, v[66:67]
	v_lshl_add_u64 v[10:11], v[8:9], 0, s[78:79]
	global_load_dword v178, v[10:11], off
	v_lshl_add_u64 v[10:11], v[8:9], 0, s[50:51]
	v_lshl_add_u64 v[8:9], v[8:9], 0, s[52:53]
	s_add_i32 s42, s42, s58
	global_load_dword v179, v[10:11], off
	global_load_dword v180, v[8:9], off
	v_mad_i64_i32 v[8:9], s[54:55], s42, v205, v[66:67]
	v_lshl_add_u64 v[10:11], v[8:9], 0, s[78:79]
	global_load_dword v181, v[10:11], off
	v_lshl_add_u64 v[10:11], v[8:9], 0, s[50:51]
	v_lshl_add_u64 v[8:9], v[8:9], 0, s[52:53]
	global_load_dword v182, v[10:11], off
	global_load_dword v191, v[8:9], off
	s_waitcnt vmcnt(31)
	v_lshlrev_b32_e32 v86, 16, v88
	v_and_b32_e32 v87, 0xffff0000, v88
	v_lshlrev_b32_e32 v88, 16, v89
	v_and_b32_e32 v89, 0xffff0000, v89
	s_waitcnt vmcnt(30)
	v_lshlrev_b32_e32 v90, 16, v92
	v_and_b32_e32 v91, 0xffff0000, v92
	v_lshlrev_b32_e32 v92, 16, v93
	v_and_b32_e32 v93, 0xffff0000, v93
	s_waitcnt vmcnt(29)
	v_lshlrev_b32_e32 v94, 16, v96
	v_and_b32_e32 v95, 0xffff0000, v96
	v_lshlrev_b32_e32 v96, 16, v97
	v_and_b32_e32 v97, 0xffff0000, v97
	s_waitcnt vmcnt(28)
	v_lshlrev_b32_e32 v98, 16, v100
	v_and_b32_e32 v99, 0xffff0000, v100
	v_lshlrev_b32_e32 v100, 16, v101
	v_and_b32_e32 v101, 0xffff0000, v101
	s_waitcnt vmcnt(27)
	v_lshlrev_b32_e32 v102, 16, v104
	v_and_b32_e32 v103, 0xffff0000, v104
	v_lshlrev_b32_e32 v104, 16, v105
	v_and_b32_e32 v105, 0xffff0000, v105
	s_waitcnt vmcnt(26)
	v_lshlrev_b32_e32 v106, 16, v108
	v_and_b32_e32 v107, 0xffff0000, v108
	v_lshlrev_b32_e32 v108, 16, v109
	v_and_b32_e32 v109, 0xffff0000, v109
	s_waitcnt vmcnt(25)
	v_lshlrev_b32_e32 v110, 16, v112
	v_and_b32_e32 v111, 0xffff0000, v112
	v_lshlrev_b32_e32 v112, 16, v113
	v_and_b32_e32 v113, 0xffff0000, v113
	s_waitcnt vmcnt(24)
	v_lshlrev_b32_e32 v114, 16, v116
	v_and_b32_e32 v115, 0xffff0000, v116
	v_lshlrev_b32_e32 v116, 16, v117
	v_and_b32_e32 v117, 0xffff0000, v117
	v_mul_f32_e64 v8, v147, -v64
	v_mul_f32_e32 v8, 0x3fb8aa3b, v8
	v_exp_f32_e32 v183, v8
	v_mul_f32_e64 v8, v149, -v64
	v_mul_f32_e32 v8, 0x3fb8aa3b, v8
	v_exp_f32_e32 v184, v8
	v_mul_f32_e64 v8, v150, -v64
	v_mul_f32_e32 v8, 0x3fb8aa3b, v8
	v_exp_f32_e32 v185, v8
	v_mul_f32_e64 v8, v151, -v64
	v_mul_f32_e32 v8, 0x3fb8aa3b, v8
	v_exp_f32_e32 v186, v8
	v_mul_f32_e64 v8, v152, -v64
	v_mul_f32_e32 v8, 0x3fb8aa3b, v8
	v_exp_f32_e32 v187, v8
	v_mul_f32_e64 v8, v153, -v64
	v_mul_f32_e32 v8, 0x3fb8aa3b, v8
	v_exp_f32_e32 v188, v8
	v_mul_f32_e64 v8, v154, -v64
	v_mul_f32_e32 v8, 0x3fb8aa3b, v8
	v_exp_f32_e32 v189, v8
	v_mul_f32_e64 v8, v155, -v64
	v_mul_f32_e32 v8, 0x3fb8aa3b, v8
	v_exp_f32_e32 v190, v8
	s_cmp_lg_u32 s43, 1
	s_mov_b32 s42, 6
	s_cselect_b64 s[54:55], -1, 0
	v_readlane_b32 s43, v241, 53
	s_branch .LBB0_704

.LBB0_742:
	v_add_u32_e32 v8, s91, v8
	v_cvt_pk_bf16_f32 v20, v13, v10
	v_lshlrev_b32_e32 v10, 4, v8
	v_and_b32_e32 v10, 0xfffffc00, v10
	v_bitop3_b32 v8, v8, v9, 56 bitop3:0x6c
	v_add3_u32 v8, v11, v10, v8
	v_cvt_pk_bf16_f32 v21, v14, v15
	ds_write_b64 v8, v[20:21]
	s_waitcnt lgkmcnt(0)
	s_barrier
	v_add_u32_e32 v8, s27, v12
	v_add_u32_e32 v12, s33, v12
	v_add_u32_e32 v125, s97, v18
	ds_read_b128 v[8:11], v8
	ds_read_b128 v[12:15], v12
	ds_read_b128 v[20:23], v17
	ds_read_b128 v[24:27], v125
	ds_read_b128 v[28:31], v125 offset:4096
	ds_read_b128 v[32:35], v125 offset:8192
	ds_read_b128 v[36:39], v125 offset:12288
	ds_read_b128 v[40:43], v17 offset:1024
	ds_read_b128 v[44:47], v125 offset:1024
	ds_read_b128 v[48:51], v125 offset:5120
	ds_read_b128 v[52:55], v125 offset:9216
	ds_read_b128 v[56:59], v125 offset:13312
	v_add_u32_e32 v127, s3, v18
	v_add_u32_e32 v144, s62, v18
	v_add_u32_e32 v145, s61, v18
	ds_read_b128 v[60:63], v17 offset:2048
	ds_read_b128 v[128:131], v125 offset:2048
	ds_read_b128 v[132:135], v125 offset:6144
	ds_read_b128 v[136:139], v125 offset:10240
	ds_read_b128 v[140:143], v125 offset:14336
	s_waitcnt lgkmcnt(13)
	v_mfma_f32_16x16x32_bf16 v[24:27], v[24:27], v[20:23], 0
	s_waitcnt lgkmcnt(12)
	v_mfma_f32_16x16x32_bf16 v[28:31], v[28:31], v[20:23], 0
	s_waitcnt lgkmcnt(11)
	v_mfma_f32_16x16x32_bf16 v[32:35], v[32:35], v[20:23], 0
	s_waitcnt lgkmcnt(10)
	v_mfma_f32_16x16x32_bf16 v[18:21], v[36:39], v[20:23], 0
	s_waitcnt lgkmcnt(8)
	v_mfma_f32_16x16x32_bf16 v[22:25], v[44:47], v[40:43], v[24:27]
	ds_read_b128 v[36:39], v17 offset:3072
	s_waitcnt lgkmcnt(8)
	v_mfma_f32_16x16x32_bf16 v[26:29], v[48:51], v[40:43], v[28:31]
	s_waitcnt lgkmcnt(7)
	v_mfma_f32_16x16x32_bf16 v[30:33], v[52:55], v[40:43], v[32:35]
	ds_read_b128 v[44:47], v125 offset:3072
	ds_read_b128 v[48:51], v125 offset:7168
	ds_read_b128 v[52:55], v125 offset:11264
	ds_read_b128 v[192:195], v125 offset:15360
	s_waitcnt lgkmcnt(10)
	v_mfma_f32_16x16x32_bf16 v[18:21], v[56:59], v[40:43], v[18:21]
	s_waitcnt lgkmcnt(8)
	v_mfma_f32_16x16x32_bf16 v[22:25], v[128:131], v[60:63], v[22:25]
	ds_read_b128 v[40:43], v127
	ds_read_b128 v[56:59], v145 offset:49152
	s_waitcnt lgkmcnt(9)
	v_mfma_f32_16x16x32_bf16 v[26:29], v[132:135], v[60:63], v[26:29]
	s_waitcnt lgkmcnt(8)
	v_mfma_f32_16x16x32_bf16 v[30:33], v[136:139], v[60:63], v[30:33]
	ds_read_b128 v[128:131], v145 offset:51200
	ds_read_b128 v[132:135], v145 offset:53248
	ds_read_b128 v[136:139], v145 offset:55296
	s_waitcnt lgkmcnt(10)
	v_mfma_f32_16x16x32_bf16 v[18:21], v[140:143], v[60:63], v[18:21]
	s_waitcnt lgkmcnt(8)
	v_mfma_f32_16x16x32_bf16 v[22:25], v[44:47], v[36:39], v[22:25]
	s_waitcnt lgkmcnt(7)
	v_mfma_f32_16x16x32_bf16 v[26:29], v[48:51], v[36:39], v[26:29]
	ds_read_b128 v[44:47], v127 offset:1024
	ds_read_b128 v[48:51], v145 offset:50176
	s_waitcnt lgkmcnt(8)
	v_mfma_f32_16x16x32_bf16 v[30:33], v[52:55], v[36:39], v[30:33]
	ds_read_b128 v[52:55], v145 offset:52224
	ds_read_b128 v[140:143], v145 offset:54272
	ds_read_b128 v[212:215], v145 offset:56320
	s_waitcnt lgkmcnt(10)
	v_mfma_f32_16x16x32_bf16 v[18:21], v[192:195], v[36:39], v[18:21]
	s_waitcnt lgkmcnt(7)
	v_mfma_f32_16x16x32_bf16 v[26:29], v[128:131], v[40:43], v[26:29]
	ds_read_b128 v[128:131], v144 offset:32768
	ds_read_b128 v[192:195], v144 offset:33792
	s_waitcnt lgkmcnt(8)
	v_mfma_f32_16x16x32_bf16 v[30:33], v[132:135], v[40:43], v[30:33]
	ds_read_b128 v[34:37], v16 offset:49152
	ds_read_b128 v[132:135], v16 offset:50176
	ds_read_b128 v[216:219], v16 offset:51200
	ds_read_b128 v[220:223], v16 offset:52224
	v_mfma_f32_16x16x32_bf16 v[22:25], v[56:59], v[40:43], v[22:25]
	s_waitcnt lgkmcnt(11)
	v_mfma_f32_16x16x32_bf16 v[18:21], v[136:139], v[40:43], v[18:21]
	s_waitcnt lgkmcnt(9)
	v_mfma_f32_16x16x32_bf16 v[60:63], v[48:51], v[44:47], v[22:25]
	s_waitcnt lgkmcnt(8)
	v_mfma_f32_16x16x32_bf16 v[56:59], v[52:55], v[44:47], v[26:29]
	s_waitcnt lgkmcnt(7)
	v_mfma_f32_16x16x32_bf16 v[48:51], v[140:143], v[44:47], v[30:33]
	ds_read_b128 v[22:25], v16 offset:53248
	ds_read_b128 v[26:29], v16 offset:54272
	ds_read_b128 v[136:139], v16 offset:55296
	ds_read_b128 v[140:143], v16 offset:56320
	s_waitcnt lgkmcnt(10)
	v_mfma_f32_16x16x32_bf16 v[52:55], v[212:215], v[44:47], v[18:21]
	s_waitcnt lgkmcnt(7)
	v_mfma_f32_16x16x32_bf16 v[18:21], v[128:131], v[34:37], 0
	s_waitcnt lgkmcnt(6)
	v_mfma_f32_16x16x32_bf16 v[44:47], v[192:195], v[132:135], v[18:21]
	s_waitcnt lgkmcnt(5)
	v_mfma_f32_16x16x32_bf16 v[18:21], v[128:131], v[216:219], 0
	s_waitcnt lgkmcnt(4)
	v_mfma_f32_16x16x32_bf16 v[40:43], v[192:195], v[220:223], v[18:21]
	s_waitcnt lgkmcnt(3)
	v_mfma_f32_16x16x32_bf16 v[18:21], v[128:131], v[22:25], 0
	s_waitcnt lgkmcnt(2)
	v_mfma_f32_16x16x32_bf16 v[32:35], v[192:195], v[26:29], v[18:21]
	s_nop 5
	ds_read_b128 v[18:21], v16 offset:57344
	ds_read_b128 v[22:25], v16 offset:58368
	ds_read_b128 v[132:135], v16 offset:59392
	ds_read_b128 v[212:215], v16 offset:60416
	s_waitcnt lgkmcnt(5)
	v_mfma_f32_16x16x32_bf16 v[26:29], v[128:131], v[136:139], 0
	ds_read_b128 v[136:139], v16 offset:61440
	ds_read_b128 v[216:219], v16 offset:62464
	ds_read_b128 v[220:223], v16 offset:63488
	ds_read_b128 v[224:227], v16 offset:64512
	s_waitcnt lgkmcnt(8)
	v_mfma_f32_16x16x32_bf16 v[36:39], v[192:195], v[140:143], v[26:29]
	s_waitcnt lgkmcnt(7)
	v_mfma_f32_16x16x32_bf16 v[16:19], v[128:131], v[18:21], 0
	s_mov_b64 s[58:59], -1
	s_andn2_b64 vcc, exec, s[56:57]
	s_waitcnt lgkmcnt(6)
	v_mfma_f32_16x16x32_bf16 v[28:31], v[192:195], v[22:25], v[16:19]
	s_waitcnt lgkmcnt(5)
	v_mfma_f32_16x16x32_bf16 v[16:19], v[128:131], v[132:135], 0
	s_waitcnt lgkmcnt(4)
	v_mfma_f32_16x16x32_bf16 v[24:27], v[192:195], v[212:215], v[16:19]
	s_waitcnt lgkmcnt(3)
	v_mfma_f32_16x16x32_bf16 v[16:19], v[128:131], v[136:139], 0
	s_waitcnt lgkmcnt(2)
	v_mfma_f32_16x16x32_bf16 v[20:23], v[192:195], v[216:219], v[16:19]
	s_waitcnt lgkmcnt(1)
	v_mfma_f32_16x16x32_bf16 v[16:19], v[128:131], v[220:223], 0
	s_waitcnt lgkmcnt(0)
	v_mfma_f32_16x16x32_bf16 v[16:19], v[192:195], v[224:227], v[16:19]
	s_cbranch_vccnz .LBB0_746
	s_waitcnt vmcnt(1)
	v_lshlrev_b32_e32 v128, 16, v0
	v_and_b32_e32 v129, 0xffff0000, v0
	v_lshlrev_b32_e32 v130, 16, v1
	v_and_b32_e32 v131, 0xffff0000, v1
	v_pk_add_f32 v[142:143], v[62:63], v[130:131]
	v_pk_add_f32 v[144:145], v[60:61], v[128:129]
	v_mul_f32_e32 v127, v143, v143
	v_mul_f32_e32 v125, v145, v145
	v_lshlrev_b32_e32 v128, 16, v2
	v_and_b32_e32 v129, 0xffff0000, v2
	v_lshlrev_b32_e32 v130, 16, v3
	v_and_b32_e32 v131, 0xffff0000, v3
	v_fmac_f32_e32 v125, v144, v144
	v_fmac_f32_e32 v127, v142, v142
	v_pk_add_f32 v[136:137], v[58:59], v[130:131]
	v_pk_add_f32 v[138:139], v[56:57], v[128:129]
	v_add_f32_e32 v125, v125, v127
	v_mul_f32_e32 v127, v139, v139
	v_mul_f32_e32 v128, v137, v137
	v_fmac_f32_e32 v127, v138, v138
	v_fmac_f32_e32 v128, v136, v136
	v_add_f32_e32 v127, v127, v128
	s_waitcnt vmcnt(0)
	v_lshlrev_b32_e32 v128, 16, v4
	v_and_b32_e32 v129, 0xffff0000, v4
	v_lshlrev_b32_e32 v130, 16, v5
	v_and_b32_e32 v131, 0xffff0000, v5
	v_pk_add_f32 v[132:133], v[50:51], v[130:131]
	v_pk_add_f32 v[134:135], v[48:49], v[128:129]
	v_add_f32_e32 v125, v125, v127
	v_mul_f32_e32 v127, v135, v135
	v_mul_f32_e32 v128, v133, v133
	v_fmac_f32_e32 v127, v134, v134
	v_fmac_f32_e32 v128, v132, v132
	v_add_f32_e32 v127, v127, v128
	v_lshlrev_b32_e32 v130, 16, v6
	v_and_b32_e32 v131, 0xffff0000, v6
	v_lshlrev_b32_e32 v128, 16, v7
	v_and_b32_e32 v129, 0xffff0000, v7
	v_pk_add_f32 v[128:129], v[54:55], v[128:129]
	v_pk_add_f32 v[130:131], v[52:53], v[130:131]
	v_add_f32_e32 v125, v125, v127
	v_mul_f32_e32 v127, v131, v131
	v_mul_f32_e32 v140, v129, v129
	v_fmac_f32_e32 v127, v130, v130
	v_fmac_f32_e32 v140, v128, v128
	v_add_f32_e32 v127, v127, v140
	v_add_f32_e32 v125, v125, v127
	v_lshlrev_b32_e32 v127, 2, v190
	v_xor_b32_e32 v140, 64, v127
	ds_bpermute_b32 v140, v140, v125
	v_xor_b32_e32 v127, 0x80, v127
	v_cmp_gt_u32_e32 vcc, 16, v190
	s_and_b32 s43, s83, 0x80
	s_waitcnt lgkmcnt(0)
	v_add_f32_e32 v125, v125, v140
	ds_bpermute_b32 v127, v127, v125
	s_waitcnt lgkmcnt(0)
	v_add_f32_e32 v125, v125, v127
	s_and_saveexec_b64 s[58:59], vcc
	s_add_i32 s49, s43, s25
	v_or_b32_e32 v127, s49, v64
	v_lshl_add_u32 v127, v127, 2, s24
	ds_write_b32 v127, v125
	s_or_b64 exec, exec, s[58:59]
	s_add_i32 s43, s43, s82
	v_or_b32_e32 v64, s43, v64
	s_waitcnt lgkmcnt(0)
	s_barrier
	v_lshl_add_u32 v64, v64, 2, s24
	ds_read_b32 v64, v64
	v_ashrrev_i32_e32 v127, 31, v126
	v_lshlrev_b64 v[126:127], 11, v[126:127]
	v_lshl_add_u64 v[126:127], s[46:47], 0, v[126:127]
	s_mov_b64 s[58:59], 0
	s_waitcnt lgkmcnt(0)
	v_add_f32_e32 v64, v125, v64
	v_ashrrev_i32_e32 v125, 31, v124
	v_lshlrev_b64 v[140:141], 2, v[124:125]
	v_lshl_add_u64 v[212:213], s[38:39], 0, v[140:141]
	global_load_dwordx4 v[192:195], v[212:213], off
	global_load_dwordx4 v[216:219], v[212:213], off offset:64
	global_load_dwordx4 v[220:223], v[212:213], off offset:128
	v_lshl_add_u64 v[224:225], s[40:41], 0, v[140:141]
	global_load_dwordx4 v[224:227], v[224:225], off
	v_fmamk_f32 v64, v64, 0x3c000000, v200
	v_rsq_f32_e32 v64, v64
	v_lshlrev_b64 v[124:125], 1, v[124:125]
	v_pk_mul_f32 v[142:143], v[142:143], v[64:65] op_sel_hi:[1,0]
	v_pk_mul_f32 v[144:145], v[144:145], v[64:65] op_sel_hi:[1,0]
	v_pk_mul_f32 v[138:139], v[138:139], v[64:65] op_sel_hi:[1,0]
	v_pk_mul_f32 v[136:137], v[136:137], v[64:65] op_sel_hi:[1,0]
	v_pk_mul_f32 v[132:133], v[132:133], v[64:65] op_sel_hi:[1,0]
	v_pk_mul_f32 v[134:135], v[134:135], v[64:65] op_sel_hi:[1,0]
	v_pk_mul_f32 v[130:131], v[130:131], v[64:65] op_sel_hi:[1,0]
	v_pk_mul_f32 v[128:129], v[128:129], v[64:65] op_sel_hi:[1,0]
	s_waitcnt vmcnt(3)
	v_pk_mul_f32 v[142:143], v[194:195], v[142:143]
	v_pk_mul_f32 v[144:145], v[192:193], v[144:145]
	v_lshlrev_b32_e32 v192, 16, v90
	v_and_b32_e32 v193, 0xffff0000, v90
	v_lshlrev_b32_e32 v194, 16, v91
	v_and_b32_e32 v195, 0xffff0000, v91
	v_pk_mul_f32 v[142:143], v[142:143], v[194:195]
	v_pk_mul_f32 v[144:145], v[144:145], v[192:193]
	s_nop 0
	v_cvt_pk_bf16_f32 v144, v144, v145
	v_cvt_pk_bf16_f32 v145, v142, v143
	v_lshl_add_u64 v[142:143], s[0:1], 1, v[126:127]
	v_lshl_add_u64 v[192:193], v[142:143], 0, v[124:125]
	global_store_dwordx2 v[192:193], v[144:145], off
	v_lshl_add_u64 v[126:127], s[22:23], 1, v[126:127]
	v_lshl_add_u64 v[124:125], v[126:127], 0, v[124:125]
	s_waitcnt vmcnt(3)
	v_pk_mul_f32 v[138:139], v[216:217], v[138:139]
	v_lshlrev_b32_e32 v142, 16, v88
	v_and_b32_e32 v143, 0xffff0000, v88
	v_pk_mul_f32 v[136:137], v[218:219], v[136:137]
	v_lshlrev_b32_e32 v144, 16, v89
	v_and_b32_e32 v145, 0xffff0000, v89
	v_pk_mul_f32 v[138:139], v[138:139], v[142:143]
	v_pk_mul_f32 v[136:137], v[136:137], v[144:145]
	v_cvt_pk_bf16_f32 v138, v138, v139
	s_nop 0
	v_cvt_pk_bf16_f32 v139, v136, v137
	global_store_dwordx2 v[192:193], v[138:139], off offset:32
	s_waitcnt vmcnt(3)
	v_pk_mul_f32 v[132:133], v[132:133], v[222:223]
	v_pk_mul_f32 v[134:135], v[134:135], v[220:221]
	v_lshlrev_b32_e32 v136, 16, v86
	v_and_b32_e32 v137, 0xffff0000, v86
	v_lshlrev_b32_e32 v138, 16, v87
	v_and_b32_e32 v139, 0xffff0000, v87
	v_pk_mul_f32 v[132:133], v[132:133], v[138:139]
	v_pk_mul_f32 v[134:135], v[134:135], v[136:137]
	s_nop 0
	v_cvt_pk_bf16_f32 v134, v134, v135
	v_cvt_pk_bf16_f32 v135, v132, v133
	global_store_dwordx2 v[192:193], v[134:135], off offset:64
	s_waitcnt vmcnt(3)
	v_pk_mul_f32 v[130:131], v[130:131], v[224:225]
	v_lshlrev_b32_e32 v132, 16, v84
	v_and_b32_e32 v133, 0xffff0000, v84
	v_pk_mul_f32 v[128:129], v[128:129], v[226:227]
	v_lshlrev_b32_e32 v134, 16, v85
	v_and_b32_e32 v135, 0xffff0000, v85
	v_pk_mul_f32 v[130:131], v[130:131], v[132:133]
	v_pk_mul_f32 v[128:129], v[128:129], v[134:135]
	v_cvt_pk_bf16_f32 v130, v130, v131
	s_nop 0
	v_cvt_pk_bf16_f32 v131, v128, v129
	global_store_dwordx2 v[124:125], v[130:131], off
